# P1 epilogue stores: default cache policy for A-mixer q/k/v column tiles (pn<24, read by next phase), nt for the rest
# speedup vs baseline: 1.0040x; 1.0040x over previous
.LBB0_194:
	v_lshl_or_b32 v20, s28, 8, v190
	v_cvt_pk_bf16_f32 v26, v26, v27
	v_cvt_pk_bf16_f32 v27, v22, v23
	v_mov_b64_e32 v[22:23], s[96:97]
	v_ashrrev_i32_e32 v21, 31, v20
	v_mad_i64_i32 v[22:23], s[30:31], v18, s51, v[22:23]
	v_cvt_pk_bf16_f32 v28, v28, v29
	v_cvt_pk_bf16_f32 v29, v24, v25
	v_lshl_add_u64 v[22:23], v[20:21], 1, v[22:23]
	s_cmp_lt_i32 s28, 24
	s_cbranch_scc1 .Lp1st_0
	global_store_dwordx4 v[22:23], v[26:29], off nt
	s_branch .Lp1sj_0
.Lp1st_0:
	global_store_dwordx4 v[22:23], v[26:29], off
.Lp1sj_0:
	v_pk_mul_f32 v[24:25], v[152:153], s[18:19] op_sel_hi:[1,0]
	s_and_b64 vcc, exec, s[6:7]
	v_pk_mul_f32 v[28:29], v[150:151], s[18:19] op_sel_hi:[1,0]
	v_pk_mul_f32 v[26:27], v[148:149], s[18:19] op_sel_hi:[1,0]
	v_pk_mul_f32 v[30:31], v[146:147], s[18:19] op_sel_hi:[1,0]
	s_cbranch_vccnz .LBB0_196
	v_and_b32_e32 v19, 64, v195
	v_xor_b32_e32 v0, 32, v195
	v_add_u32_e32 v19, 64, v19
	v_cmp_lt_i32_e32 vcc, v0, v19
	s_waitcnt vmcnt(0)
	v_pk_mul_f32 v[14:15], v[28:29], v[14:15]
	v_mul_f32_e32 v16, v24, v16
	v_cndmask_b32_e32 v0, v195, v0, vcc
	v_lshlrev_b32_e32 v0, 2, v0
	ds_bpermute_b32 v32, v0, v28
	ds_bpermute_b32 v33, v0, v29
	ds_bpermute_b32 v19, v0, v24
	ds_bpermute_b32 v146, v0, v30
	ds_bpermute_b32 v147, v0, v31
	v_mul_f32_e32 v4, v26, v4
	s_waitcnt lgkmcnt(3)
	v_pk_mul_f32 v[28:29], v[170:171], v[32:33]
	ds_bpermute_b32 v32, v0, v26
	s_waitcnt lgkmcnt(3)
	v_mul_f32_e32 v19, v170, v19
	v_mul_f32_e32 v24, v12, v19
	ds_bpermute_b32 v12, v0, v25
	ds_bpermute_b32 v0, v0, v27
	s_waitcnt lgkmcnt(2)
	v_mul_f32_e32 v19, v170, v32
	v_mul_f32_e32 v26, v8, v19
	v_mov_b32_e32 v32, v17
	s_waitcnt lgkmcnt(1)
	v_mul_f32_e32 v33, v170, v12
	v_mov_b32_e32 v12, v25
	v_pk_fma_f32 v[28:29], v[10:11], v[28:29], v[14:15]
	s_waitcnt lgkmcnt(0)
	v_mul_f32_e32 v11, v170, v0
	v_mov_b32_e32 v8, v27
	v_mov_b32_e32 v10, v5
	v_pk_mul_f32 v[12:13], v[12:13], v[32:33]
	v_pk_mul_f32 v[8:9], v[8:9], v[10:11]
	v_pk_mul_f32 v[2:3], v[30:31], v[2:3]
	v_pk_mul_f32 v[30:31], v[170:171], v[146:147]
	v_mov_b32_e32 v17, v12
	v_mov_b32_e32 v25, v13
	v_mov_b32_e32 v5, v8
	v_mov_b32_e32 v27, v9
	v_pk_add_f32 v[24:25], v[16:17], v[24:25]
	v_pk_fma_f32 v[30:31], v[6:7], v[30:31], v[2:3]
	v_pk_add_f32 v[26:27], v[4:5], v[26:27]
.LBB0_196:
	v_cvt_pk_bf16_f32 v2, v28, v29
	v_cvt_pk_bf16_f32 v3, v24, v25
	v_cvt_pk_bf16_f32 v4, v30, v31
	v_cvt_pk_bf16_f32 v5, v26, v27
	s_cmp_lt_i32 s28, 24
	s_cbranch_scc1 .Lp1st_1
	global_store_dwordx4 v[22:23], v[2:5], off offset:256 nt
	s_branch .Lp1sj_1
.Lp1st_1:
	global_store_dwordx4 v[22:23], v[2:5], off offset:256
.Lp1sj_1:
	v_or_b32_e32 v22, 16, v18
	s_and_b64 vcc, exec, s[6:7]
	v_ashrrev_i32_e32 v23, 31, v22
	s_cbranch_vccnz .LBB0_198
	v_lshlrev_b64 v[2:3], 6, v[22:23]
	v_lshl_add_u64 v[6:7], v[172:173], 0, v[2:3]
	v_lshl_add_u64 v[8:9], v[174:175], 0, v[2:3]
	global_load_dwordx4 v[2:5], v[6:7], off offset:16
	global_load_dwordx4 v[14:17], v[6:7], off
	global_load_dwordx4 v[10:13], v[8:9], off
	s_nop 0
	global_load_dwordx4 v[6:9], v[8:9], off offset:16
	s_branch .LBB0_199

.LBB0_201:
	v_cvt_pk_bf16_f32 v28, v28, v29
	v_cvt_pk_bf16_f32 v29, v24, v25
	v_mov_b64_e32 v[24:25], s[96:97]
	v_mad_i64_i32 v[22:23], s[30:31], v22, s51, v[24:25]
	v_cvt_pk_bf16_f32 v30, v30, v31
	v_cvt_pk_bf16_f32 v31, v26, v27
	v_lshl_add_u64 v[22:23], v[20:21], 1, v[22:23]
	s_cmp_lt_i32 s28, 24
	s_cbranch_scc1 .Lp1st_2
	global_store_dwordx4 v[22:23], v[28:31], off nt
	s_branch .Lp1sj_2
.Lp1st_2:
	global_store_dwordx4 v[22:23], v[28:31], off
.Lp1sj_2:
	v_pk_mul_f32 v[24:25], v[136:137], s[18:19] op_sel_hi:[1,0]
	v_pk_mul_f32 v[26:27], v[132:133], s[18:19] op_sel_hi:[1,0]
	v_pk_mul_f32 v[28:29], v[134:135], s[18:19] op_sel_hi:[1,0]
	s_and_b64 vcc, exec, s[6:7]
	v_pk_mul_f32 v[30:31], v[130:131], s[18:19] op_sel_hi:[1,0]
	s_cbranch_vccnz .LBB0_203
	v_and_b32_e32 v19, 64, v195
	v_xor_b32_e32 v0, 32, v195
	v_add_u32_e32 v19, 64, v19
	v_cmp_lt_i32_e32 vcc, v0, v19
	s_waitcnt vmcnt(3)
	v_pk_mul_f32 v[14:15], v[28:29], v[14:15]
	v_mul_f32_e32 v16, v24, v16
	v_cndmask_b32_e32 v0, v195, v0, vcc
	v_lshlrev_b32_e32 v0, 2, v0
	ds_bpermute_b32 v32, v0, v28
	ds_bpermute_b32 v33, v0, v29
	ds_bpermute_b32 v19, v0, v24
	ds_bpermute_b32 v130, v0, v30
	ds_bpermute_b32 v131, v0, v31
	v_mul_f32_e32 v4, v26, v4
	s_waitcnt lgkmcnt(3)
	v_pk_mul_f32 v[28:29], v[170:171], v[32:33]
	ds_bpermute_b32 v32, v0, v26
	s_waitcnt lgkmcnt(3)
	v_mul_f32_e32 v19, v170, v19
	s_waitcnt vmcnt(2)
	v_mul_f32_e32 v24, v12, v19
	ds_bpermute_b32 v12, v0, v25
	ds_bpermute_b32 v0, v0, v27
	s_waitcnt lgkmcnt(2)
	v_mul_f32_e32 v19, v170, v32
	s_waitcnt vmcnt(1)
	v_mul_f32_e32 v26, v8, v19
	v_mov_b32_e32 v32, v17
	s_waitcnt lgkmcnt(1)
	v_mul_f32_e32 v33, v170, v12
	v_mov_b32_e32 v12, v25
	v_pk_fma_f32 v[28:29], v[10:11], v[28:29], v[14:15]
	s_waitcnt lgkmcnt(0)
	v_mul_f32_e32 v11, v170, v0
	v_mov_b32_e32 v8, v27
	v_mov_b32_e32 v10, v5
	v_pk_mul_f32 v[12:13], v[12:13], v[32:33]
	v_pk_mul_f32 v[8:9], v[8:9], v[10:11]
	v_pk_mul_f32 v[2:3], v[30:31], v[2:3]
	v_pk_mul_f32 v[30:31], v[170:171], v[130:131]
	v_mov_b32_e32 v17, v12
	v_mov_b32_e32 v25, v13
	v_mov_b32_e32 v5, v8
	v_mov_b32_e32 v27, v9
	v_pk_add_f32 v[24:25], v[16:17], v[24:25]
	v_pk_fma_f32 v[30:31], v[6:7], v[30:31], v[2:3]
	v_pk_add_f32 v[26:27], v[4:5], v[26:27]

.Lp1sj_3:
	v_or_b32_e32 v22, 32, v18
	s_and_b64 vcc, exec, s[6:7]
	v_ashrrev_i32_e32 v23, 31, v22
	s_cbranch_vccnz .LBB0_205
	v_lshlrev_b64 v[2:3], 6, v[22:23]
	s_waitcnt vmcnt(2)
	v_lshl_add_u64 v[6:7], v[172:173], 0, v[2:3]
	v_lshl_add_u64 v[8:9], v[174:175], 0, v[2:3]
	global_load_dwordx4 v[2:5], v[6:7], off offset:16
	global_load_dwordx4 v[14:17], v[6:7], off
	global_load_dwordx4 v[10:13], v[8:9], off
	s_nop 0
	global_load_dwordx4 v[6:9], v[8:9], off offset:16
	s_branch .LBB0_206

.Lp1sj_4:
	v_pk_mul_f32 v[24:25], v[120:121], s[18:19] op_sel_hi:[1,0]
	v_pk_mul_f32 v[26:27], v[116:117], s[18:19] op_sel_hi:[1,0]
	v_pk_mul_f32 v[28:29], v[118:119], s[18:19] op_sel_hi:[1,0]
	s_and_b64 vcc, exec, s[6:7]
	v_pk_mul_f32 v[30:31], v[114:115], s[18:19] op_sel_hi:[1,0]
	s_cbranch_vccnz .LBB0_210
	v_and_b32_e32 v19, 64, v195
	v_xor_b32_e32 v0, 32, v195
	v_add_u32_e32 v19, 64, v19
	v_cmp_lt_i32_e32 vcc, v0, v19
	s_waitcnt vmcnt(3)
	v_pk_mul_f32 v[14:15], v[28:29], v[14:15]
	v_mul_f32_e32 v16, v24, v16
	v_cndmask_b32_e32 v0, v195, v0, vcc
	v_lshlrev_b32_e32 v0, 2, v0
	ds_bpermute_b32 v32, v0, v28
	ds_bpermute_b32 v33, v0, v29
	ds_bpermute_b32 v19, v0, v24
	ds_bpermute_b32 v114, v0, v30
	ds_bpermute_b32 v115, v0, v31
	v_mul_f32_e32 v4, v26, v4
	s_waitcnt lgkmcnt(3)
	v_pk_mul_f32 v[28:29], v[170:171], v[32:33]
	ds_bpermute_b32 v32, v0, v26
	s_waitcnt lgkmcnt(3)
	v_mul_f32_e32 v19, v170, v19
	s_waitcnt vmcnt(2)
	v_mul_f32_e32 v24, v12, v19
	ds_bpermute_b32 v12, v0, v25
	ds_bpermute_b32 v0, v0, v27
	s_waitcnt lgkmcnt(2)
	v_mul_f32_e32 v19, v170, v32
	s_waitcnt vmcnt(1)
	v_mul_f32_e32 v26, v8, v19
	v_mov_b32_e32 v32, v17
	s_waitcnt lgkmcnt(1)
	v_mul_f32_e32 v33, v170, v12
	v_mov_b32_e32 v12, v25
	v_pk_fma_f32 v[28:29], v[10:11], v[28:29], v[14:15]
	s_waitcnt lgkmcnt(0)
	v_mul_f32_e32 v11, v170, v0
	v_mov_b32_e32 v8, v27
	v_mov_b32_e32 v10, v5
	v_pk_mul_f32 v[12:13], v[12:13], v[32:33]
	v_pk_mul_f32 v[8:9], v[8:9], v[10:11]
	v_pk_mul_f32 v[2:3], v[30:31], v[2:3]
	v_pk_mul_f32 v[30:31], v[170:171], v[114:115]
	v_mov_b32_e32 v17, v12
	v_mov_b32_e32 v25, v13
	v_mov_b32_e32 v5, v8
	v_mov_b32_e32 v27, v9
	v_pk_add_f32 v[24:25], v[16:17], v[24:25]
	v_pk_fma_f32 v[30:31], v[6:7], v[30:31], v[2:3]
	v_pk_add_f32 v[26:27], v[4:5], v[26:27]

.Lp1sj_5:
	v_or_b32_e32 v22, 48, v18
	s_and_b64 vcc, exec, s[6:7]
	v_ashrrev_i32_e32 v23, 31, v22
	s_cbranch_vccnz .LBB0_212
	v_lshlrev_b64 v[2:3], 6, v[22:23]
	s_waitcnt vmcnt(2)
	v_lshl_add_u64 v[6:7], v[172:173], 0, v[2:3]
	v_lshl_add_u64 v[8:9], v[174:175], 0, v[2:3]
	global_load_dwordx4 v[2:5], v[6:7], off offset:16
	global_load_dwordx4 v[14:17], v[6:7], off
	global_load_dwordx4 v[10:13], v[8:9], off
	s_nop 0
	global_load_dwordx4 v[6:9], v[8:9], off offset:16
	s_branch .LBB0_213

.Lp1sj_6:
	v_pk_mul_f32 v[24:25], v[104:105], s[18:19] op_sel_hi:[1,0]
	v_pk_mul_f32 v[26:27], v[100:101], s[18:19] op_sel_hi:[1,0]
	v_pk_mul_f32 v[28:29], v[102:103], s[18:19] op_sel_hi:[1,0]
	s_and_b64 vcc, exec, s[6:7]
	v_pk_mul_f32 v[30:31], v[98:99], s[18:19] op_sel_hi:[1,0]
	s_cbranch_vccnz .LBB0_217
	v_and_b32_e32 v19, 64, v195
	v_xor_b32_e32 v0, 32, v195
	v_add_u32_e32 v19, 64, v19
	v_cmp_lt_i32_e32 vcc, v0, v19
	s_waitcnt vmcnt(3)
	v_pk_mul_f32 v[14:15], v[28:29], v[14:15]
	v_mul_f32_e32 v16, v24, v16
	v_cndmask_b32_e32 v0, v195, v0, vcc
	v_lshlrev_b32_e32 v0, 2, v0
	ds_bpermute_b32 v32, v0, v28
	ds_bpermute_b32 v33, v0, v29
	ds_bpermute_b32 v19, v0, v24
	ds_bpermute_b32 v98, v0, v30
	ds_bpermute_b32 v99, v0, v31
	v_mul_f32_e32 v4, v26, v4
	s_waitcnt lgkmcnt(3)
	v_pk_mul_f32 v[28:29], v[170:171], v[32:33]
	ds_bpermute_b32 v32, v0, v26
	s_waitcnt lgkmcnt(3)
	v_mul_f32_e32 v19, v170, v19
	s_waitcnt vmcnt(2)
	v_mul_f32_e32 v24, v12, v19
	ds_bpermute_b32 v12, v0, v25
	ds_bpermute_b32 v0, v0, v27
	s_waitcnt lgkmcnt(2)
	v_mul_f32_e32 v19, v170, v32
	s_waitcnt vmcnt(1)
	v_mul_f32_e32 v26, v8, v19
	v_mov_b32_e32 v32, v17
	s_waitcnt lgkmcnt(1)
	v_mul_f32_e32 v33, v170, v12
	v_mov_b32_e32 v12, v25
	v_pk_fma_f32 v[28:29], v[10:11], v[28:29], v[14:15]
	s_waitcnt lgkmcnt(0)
	v_mul_f32_e32 v11, v170, v0
	v_mov_b32_e32 v8, v27
	v_mov_b32_e32 v10, v5
	v_pk_mul_f32 v[12:13], v[12:13], v[32:33]
	v_pk_mul_f32 v[8:9], v[8:9], v[10:11]
	v_pk_mul_f32 v[2:3], v[30:31], v[2:3]
	v_pk_mul_f32 v[30:31], v[170:171], v[98:99]
	v_mov_b32_e32 v17, v12
	v_mov_b32_e32 v25, v13
	v_mov_b32_e32 v5, v8
	v_mov_b32_e32 v27, v9
	v_pk_add_f32 v[24:25], v[16:17], v[24:25]
	v_pk_fma_f32 v[30:31], v[6:7], v[30:31], v[2:3]
	v_pk_add_f32 v[26:27], v[4:5], v[26:27]

.Lp1sj_7:
	v_add_u32_e32 v22, 0x80, v18
	s_and_b64 vcc, exec, s[6:7]
	v_ashrrev_i32_e32 v23, 31, v22
	s_cbranch_vccnz .LBB0_219
	v_lshlrev_b64 v[2:3], 6, v[22:23]
	s_waitcnt vmcnt(2)
	v_lshl_add_u64 v[6:7], v[172:173], 0, v[2:3]
	v_lshl_add_u64 v[8:9], v[174:175], 0, v[2:3]
	global_load_dwordx4 v[2:5], v[6:7], off offset:16
	global_load_dwordx4 v[14:17], v[6:7], off
	global_load_dwordx4 v[10:13], v[8:9], off
	s_nop 0
	global_load_dwordx4 v[6:9], v[8:9], off offset:16
	s_branch .LBB0_220

.Lp1sj_8:
	v_pk_mul_f32 v[24:25], v[88:89], s[18:19] op_sel_hi:[1,0]
	v_pk_mul_f32 v[26:27], v[84:85], s[18:19] op_sel_hi:[1,0]
	v_pk_mul_f32 v[28:29], v[86:87], s[18:19] op_sel_hi:[1,0]
	s_and_b64 vcc, exec, s[6:7]
	v_pk_mul_f32 v[30:31], v[82:83], s[18:19] op_sel_hi:[1,0]
	s_cbranch_vccnz .LBB0_224
	v_and_b32_e32 v19, 64, v195
	v_xor_b32_e32 v0, 32, v195
	v_add_u32_e32 v19, 64, v19
	v_cmp_lt_i32_e32 vcc, v0, v19
	s_waitcnt vmcnt(3)
	v_pk_mul_f32 v[14:15], v[28:29], v[14:15]
	v_mul_f32_e32 v16, v24, v16
	v_cndmask_b32_e32 v0, v195, v0, vcc
	v_lshlrev_b32_e32 v0, 2, v0
	ds_bpermute_b32 v32, v0, v28
	ds_bpermute_b32 v33, v0, v29
	ds_bpermute_b32 v19, v0, v24
	ds_bpermute_b32 v82, v0, v30
	ds_bpermute_b32 v83, v0, v31
	v_mul_f32_e32 v4, v26, v4
	s_waitcnt lgkmcnt(3)
	v_pk_mul_f32 v[28:29], v[170:171], v[32:33]
	ds_bpermute_b32 v32, v0, v26
	s_waitcnt lgkmcnt(3)
	v_mul_f32_e32 v19, v170, v19
	s_waitcnt vmcnt(2)
	v_mul_f32_e32 v24, v12, v19
	ds_bpermute_b32 v12, v0, v25
	ds_bpermute_b32 v0, v0, v27
	s_waitcnt lgkmcnt(2)
	v_mul_f32_e32 v19, v170, v32
	s_waitcnt vmcnt(1)
	v_mul_f32_e32 v26, v8, v19
	v_mov_b32_e32 v32, v17
	s_waitcnt lgkmcnt(1)
	v_mul_f32_e32 v33, v170, v12
	v_mov_b32_e32 v12, v25
	v_pk_fma_f32 v[28:29], v[10:11], v[28:29], v[14:15]
	s_waitcnt lgkmcnt(0)
	v_mul_f32_e32 v11, v170, v0
	v_mov_b32_e32 v8, v27
	v_mov_b32_e32 v10, v5
	v_pk_mul_f32 v[12:13], v[12:13], v[32:33]
	v_pk_mul_f32 v[8:9], v[8:9], v[10:11]
	v_pk_mul_f32 v[2:3], v[30:31], v[2:3]
	v_pk_mul_f32 v[30:31], v[170:171], v[82:83]
	v_mov_b32_e32 v17, v12
	v_mov_b32_e32 v25, v13
	v_mov_b32_e32 v5, v8
	v_mov_b32_e32 v27, v9
	v_pk_add_f32 v[24:25], v[16:17], v[24:25]
	v_pk_fma_f32 v[30:31], v[6:7], v[30:31], v[2:3]
	v_pk_add_f32 v[26:27], v[4:5], v[26:27]

.Lp1sj_9:
	v_add_u32_e32 v22, 0x90, v18
	s_and_b64 vcc, exec, s[6:7]
	v_ashrrev_i32_e32 v23, 31, v22
	s_cbranch_vccnz .LBB0_226
	v_lshlrev_b64 v[2:3], 6, v[22:23]
	s_waitcnt vmcnt(2)
	v_lshl_add_u64 v[6:7], v[172:173], 0, v[2:3]
	v_lshl_add_u64 v[8:9], v[174:175], 0, v[2:3]
	global_load_dwordx4 v[2:5], v[6:7], off offset:16
	global_load_dwordx4 v[14:17], v[6:7], off
	global_load_dwordx4 v[10:13], v[8:9], off
	s_nop 0
	global_load_dwordx4 v[6:9], v[8:9], off offset:16
	s_branch .LBB0_227

.Lp1sj_10:
	v_pk_mul_f32 v[24:25], v[72:73], s[18:19] op_sel_hi:[1,0]
	v_pk_mul_f32 v[26:27], v[68:69], s[18:19] op_sel_hi:[1,0]
	v_pk_mul_f32 v[28:29], v[70:71], s[18:19] op_sel_hi:[1,0]
	s_and_b64 vcc, exec, s[6:7]
	v_pk_mul_f32 v[30:31], v[66:67], s[18:19] op_sel_hi:[1,0]
	s_cbranch_vccnz .LBB0_231
	v_and_b32_e32 v19, 64, v195
	v_xor_b32_e32 v0, 32, v195
	v_add_u32_e32 v19, 64, v19
	v_cmp_lt_i32_e32 vcc, v0, v19
	s_waitcnt vmcnt(3)
	v_pk_mul_f32 v[14:15], v[28:29], v[14:15]
	v_mul_f32_e32 v16, v24, v16
	v_cndmask_b32_e32 v0, v195, v0, vcc
	v_lshlrev_b32_e32 v0, 2, v0
	ds_bpermute_b32 v32, v0, v28
	ds_bpermute_b32 v33, v0, v29
	ds_bpermute_b32 v19, v0, v24
	ds_bpermute_b32 v66, v0, v30
	ds_bpermute_b32 v67, v0, v31
	v_mul_f32_e32 v4, v26, v4
	s_waitcnt lgkmcnt(3)
	v_pk_mul_f32 v[28:29], v[170:171], v[32:33]
	ds_bpermute_b32 v32, v0, v26
	s_waitcnt lgkmcnt(3)
	v_mul_f32_e32 v19, v170, v19
	s_waitcnt vmcnt(2)
	v_mul_f32_e32 v24, v12, v19
	ds_bpermute_b32 v12, v0, v25
	ds_bpermute_b32 v0, v0, v27
	s_waitcnt lgkmcnt(2)
	v_mul_f32_e32 v19, v170, v32
	s_waitcnt vmcnt(1)
	v_mul_f32_e32 v26, v8, v19
	v_mov_b32_e32 v32, v17
	s_waitcnt lgkmcnt(1)
	v_mul_f32_e32 v33, v170, v12
	v_mov_b32_e32 v12, v25
	v_pk_fma_f32 v[28:29], v[10:11], v[28:29], v[14:15]
	s_waitcnt lgkmcnt(0)
	v_mul_f32_e32 v11, v170, v0
	v_mov_b32_e32 v8, v27
	v_mov_b32_e32 v10, v5
	v_pk_mul_f32 v[12:13], v[12:13], v[32:33]
	v_pk_mul_f32 v[8:9], v[8:9], v[10:11]
	v_pk_mul_f32 v[2:3], v[30:31], v[2:3]
	v_pk_mul_f32 v[30:31], v[170:171], v[66:67]
	v_mov_b32_e32 v17, v12
	v_mov_b32_e32 v25, v13
	v_mov_b32_e32 v5, v8
	v_mov_b32_e32 v27, v9
	v_pk_add_f32 v[24:25], v[16:17], v[24:25]
	v_pk_fma_f32 v[30:31], v[6:7], v[30:31], v[2:3]
	v_pk_add_f32 v[26:27], v[4:5], v[26:27]

.Lp1sj_11:
	v_add_u32_e32 v22, 0xa0, v18
	s_and_b64 vcc, exec, s[6:7]
	v_ashrrev_i32_e32 v23, 31, v22
	s_cbranch_vccnz .LBB0_233
	v_lshlrev_b64 v[2:3], 6, v[22:23]
	s_waitcnt vmcnt(2)
	v_lshl_add_u64 v[6:7], v[172:173], 0, v[2:3]
	v_lshl_add_u64 v[8:9], v[174:175], 0, v[2:3]
	global_load_dwordx4 v[2:5], v[6:7], off offset:16
	global_load_dwordx4 v[14:17], v[6:7], off
	global_load_dwordx4 v[10:13], v[8:9], off
	s_nop 0
	global_load_dwordx4 v[6:9], v[8:9], off offset:16
	s_branch .LBB0_234

.Lp1sj_12:
	v_pk_mul_f32 v[24:25], v[56:57], s[18:19] op_sel_hi:[1,0]
	v_pk_mul_f32 v[26:27], v[52:53], s[18:19] op_sel_hi:[1,0]
	v_pk_mul_f32 v[28:29], v[54:55], s[18:19] op_sel_hi:[1,0]
	s_and_b64 vcc, exec, s[6:7]
	v_pk_mul_f32 v[30:31], v[50:51], s[18:19] op_sel_hi:[1,0]
	s_cbranch_vccnz .LBB0_238
	v_and_b32_e32 v19, 64, v195
	v_xor_b32_e32 v0, 32, v195
	v_add_u32_e32 v19, 64, v19
	v_cmp_lt_i32_e32 vcc, v0, v19
	s_waitcnt vmcnt(3)
	v_pk_mul_f32 v[14:15], v[28:29], v[14:15]
	v_mul_f32_e32 v16, v24, v16
	v_cndmask_b32_e32 v0, v195, v0, vcc
	v_lshlrev_b32_e32 v0, 2, v0
	ds_bpermute_b32 v32, v0, v28
	ds_bpermute_b32 v33, v0, v29
	ds_bpermute_b32 v19, v0, v24
	ds_bpermute_b32 v50, v0, v30
	ds_bpermute_b32 v51, v0, v31
	v_mul_f32_e32 v4, v26, v4
	s_waitcnt lgkmcnt(3)
	v_pk_mul_f32 v[28:29], v[170:171], v[32:33]
	ds_bpermute_b32 v32, v0, v26
	s_waitcnt lgkmcnt(3)
	v_mul_f32_e32 v19, v170, v19
	s_waitcnt vmcnt(2)
	v_mul_f32_e32 v24, v12, v19
	ds_bpermute_b32 v12, v0, v25
	ds_bpermute_b32 v0, v0, v27
	s_waitcnt lgkmcnt(2)
	v_mul_f32_e32 v19, v170, v32
	s_waitcnt vmcnt(1)
	v_mul_f32_e32 v26, v8, v19
	v_mov_b32_e32 v32, v17
	s_waitcnt lgkmcnt(1)
	v_mul_f32_e32 v33, v170, v12
	v_mov_b32_e32 v12, v25
	v_pk_fma_f32 v[28:29], v[10:11], v[28:29], v[14:15]
	s_waitcnt lgkmcnt(0)
	v_mul_f32_e32 v11, v170, v0
	v_mov_b32_e32 v8, v27
	v_mov_b32_e32 v10, v5
	v_pk_mul_f32 v[12:13], v[12:13], v[32:33]
	v_pk_mul_f32 v[8:9], v[8:9], v[10:11]
	v_pk_mul_f32 v[2:3], v[30:31], v[2:3]
	v_pk_mul_f32 v[30:31], v[170:171], v[50:51]
	v_mov_b32_e32 v17, v12
	v_mov_b32_e32 v25, v13
	v_mov_b32_e32 v5, v8
	v_mov_b32_e32 v27, v9
	v_pk_add_f32 v[24:25], v[16:17], v[24:25]
	v_pk_fma_f32 v[30:31], v[6:7], v[30:31], v[2:3]
	v_pk_add_f32 v[26:27], v[4:5], v[26:27]
.LBB0_238:
	v_add_u32_e32 v18, 0xb0, v18
	s_and_b64 vcc, exec, s[6:7]
	v_ashrrev_i32_e32 v19, 31, v18
	v_cvt_pk_bf16_f32 v2, v28, v29
	v_cvt_pk_bf16_f32 v3, v24, v25
	v_cvt_pk_bf16_f32 v4, v30, v31
	v_cvt_pk_bf16_f32 v5, v26, v27
	s_cmp_lt_i32 s28, 24
	s_cbranch_scc1 .Lp1st_13
	global_store_dwordx4 v[22:23], v[2:5], off offset:256 nt
	s_branch .Lp1sj_13

.Lp1sj_13:
	s_cbranch_vccnz .LBB0_240
	s_nop 0
	v_lshlrev_b64 v[2:3], 6, v[18:19]
	s_waitcnt vmcnt(2)
	v_lshl_add_u64 v[6:7], v[172:173], 0, v[2:3]
	v_lshl_add_u64 v[8:9], v[174:175], 0, v[2:3]
	global_load_dwordx4 v[2:5], v[6:7], off offset:16
	global_load_dwordx4 v[14:17], v[6:7], off
	global_load_dwordx4 v[10:13], v[8:9], off
	s_nop 0
	global_load_dwordx4 v[6:9], v[8:9], off offset:16
	s_branch .LBB0_241

.LBB0_243:
	v_cvt_pk_bf16_f32 v26, v26, v27
	v_cvt_pk_bf16_f32 v27, v22, v23
	v_mov_b64_e32 v[22:23], s[96:97]
	v_mad_i64_i32 v[18:19], s[30:31], v18, s51, v[22:23]
	v_lshl_add_u64 v[18:19], v[20:21], 1, v[18:19]
	v_cvt_pk_bf16_f32 v28, v28, v29
	v_cvt_pk_bf16_f32 v29, v24, v25
	s_cmp_lt_i32 s28, 24
	s_cbranch_scc1 .Lp1st_14
	global_store_dwordx4 v[18:19], v[26:29], off nt
	s_branch .Lp1sj_14
.Lp1st_14:
	global_store_dwordx4 v[18:19], v[26:29], off
.Lp1sj_14:
	v_pk_mul_f32 v[20:21], v[40:41], s[18:19] op_sel_hi:[1,0]
	v_pk_mul_f32 v[24:25], v[38:39], s[18:19] op_sel_hi:[1,0]
	v_pk_mul_f32 v[22:23], v[36:37], s[18:19] op_sel_hi:[1,0]
	s_and_b64 vcc, exec, s[6:7]
	v_pk_mul_f32 v[26:27], v[34:35], s[18:19] op_sel_hi:[1,0]
	s_cbranch_vccnz .LBB0_245
	v_and_b32_e32 v28, 64, v195
	v_xor_b32_e32 v0, 32, v195
	v_add_u32_e32 v28, 64, v28
	v_cmp_lt_i32_e32 vcc, v0, v28
	s_waitcnt vmcnt(3)
	v_pk_mul_f32 v[14:15], v[24:25], v[14:15]
	v_mul_f32_e32 v16, v20, v16
	v_cndmask_b32_e32 v0, v195, v0, vcc
	v_lshlrev_b32_e32 v0, 2, v0
	ds_bpermute_b32 v28, v0, v24
	ds_bpermute_b32 v29, v0, v25
	ds_bpermute_b32 v30, v0, v26
	ds_bpermute_b32 v31, v0, v27
	v_mul_f32_e32 v4, v22, v4
	v_pk_mul_f32 v[2:3], v[26:27], v[2:3]
	s_waitcnt lgkmcnt(2)
	v_pk_mul_f32 v[24:25], v[170:171], v[28:29]
	ds_bpermute_b32 v28, v0, v20
	ds_bpermute_b32 v29, v0, v22
	s_waitcnt vmcnt(2)
	v_pk_fma_f32 v[24:25], v[10:11], v[24:25], v[14:15]
	v_mov_b32_e32 v10, v5
	s_waitcnt lgkmcnt(2)
	v_pk_mul_f32 v[26:27], v[170:171], v[30:31]
	s_waitcnt lgkmcnt(1)
	v_mul_f32_e32 v20, v170, v28
	v_mul_f32_e32 v20, v12, v20
	ds_bpermute_b32 v12, v0, v21
	ds_bpermute_b32 v0, v0, v23
	s_waitcnt lgkmcnt(2)
	v_mul_f32_e32 v22, v170, v29
	s_waitcnt vmcnt(1)
	v_mul_f32_e32 v22, v8, v22
	v_mov_b32_e32 v28, v17
	s_waitcnt lgkmcnt(1)
	v_mul_f32_e32 v29, v170, v12
	v_mov_b32_e32 v12, v21
	s_waitcnt lgkmcnt(0)
	v_mul_f32_e32 v11, v170, v0
	v_mov_b32_e32 v8, v23
	v_pk_mul_f32 v[12:13], v[12:13], v[28:29]
	v_pk_mul_f32 v[8:9], v[8:9], v[10:11]
	v_mov_b32_e32 v17, v12
	v_mov_b32_e32 v21, v13
	v_mov_b32_e32 v5, v8
	v_mov_b32_e32 v23, v9
	v_pk_add_f32 v[20:21], v[16:17], v[20:21]
	v_pk_fma_f32 v[26:27], v[6:7], v[26:27], v[2:3]
	v_pk_add_f32 v[22:23], v[4:5], v[22:23]
.LBB0_245:
	s_andn2_b64 vcc, exec, s[4:5]
	s_mov_b64 s[4:5], -1
	v_cvt_pk_bf16_f32 v2, v24, v25
	v_cvt_pk_bf16_f32 v3, v20, v21
	v_cvt_pk_bf16_f32 v4, v26, v27
	v_cvt_pk_bf16_f32 v5, v22, v23
	s_cmp_lt_i32 s28, 24
	s_cbranch_scc1 .Lp1st_15
	global_store_dwordx4 v[18:19], v[2:5], off offset:256 nt
	s_branch .Lp1sj_15
.Lp1st_15:
	global_store_dwordx4 v[18:19], v[2:5], off offset:256
.Lp1sj_15:
	s_cbranch_vccnz .LBB0_182
	s_andn2_b64 vcc, exec, s[10:11]
	s_cbranch_vccnz .LBB0_181
	s_barrier
	s_branch .LBB0_181
